# MP0: feat-address VALU (5 ops) moved under the wave-0 branch so waves 1-7 (incl. wave 0's SIMD partner) skip it; node wave-0 block with packed converts (6 fewer VALU)
# speedup vs baseline: 1.0016x; 1.0016x over previous
.LBB5_14:
	v_or_b32_e32 v0, s33, v200
	ds_read_b128 v[142:145], v0 offset:0
	s_waitcnt lgkmcnt(4)
	s_nop 0
	v_mfma_f32_16x16x32_f16 v[134:137], v[114:117], v[134:137], v[166:169]
	ds_read_b128 v[146:149], v0 offset:0x1000
	s_waitcnt lgkmcnt(4)
	s_nop 0
	v_mfma_f32_16x16x32_f16 v[138:141], v[114:117], v[138:141], v[170:173]
	ds_read_b128 v[150:153], v0 offset:0x2000
	s_waitcnt lgkmcnt(4)
	s_nop 0
	v_mfma_f32_16x16x32_f16 v[154:157], v[114:117], v[158:161], v[174:177]
	ds_read_b128 v[158:161], v0 offset:0x3000
	s_waitcnt lgkmcnt(4)
	s_nop 0
	v_mfma_f32_16x16x32_f16 v[162:165], v[114:117], v[162:165], v[178:181]
	ds_read_b128 v[166:169], v205 offset:0
	s_waitcnt lgkmcnt(4)
	s_nop 0
	v_mfma_f32_16x16x32_f16 v[134:137], v[106:109], v[142:145], v[134:137]
	ds_read_b128 v[142:145], v205 offset:0x100
	s_waitcnt lgkmcnt(4)
	s_nop 0
	v_mfma_f32_16x16x32_f16 v[138:141], v[106:109], v[146:149], v[138:141]
	ds_read_b128 v[146:149], v205 offset:0x200
	s_waitcnt lgkmcnt(4)
	s_nop 0
	v_mfma_f32_16x16x32_f16 v[150:153], v[106:109], v[150:153], v[154:157]
	ds_read_b128 v[154:157], v205 offset:0x300
	s_waitcnt lgkmcnt(4)
	s_nop 0
	v_mfma_f32_16x16x32_f16 v[158:161], v[106:109], v[158:161], v[162:165]
	s_waitcnt lgkmcnt(3)
	s_nop 0
	v_mfma_f32_16x16x32_f16 v[134:137], v[102:105], v[166:169], v[134:137]
	s_waitcnt lgkmcnt(2)
	s_nop 0
	v_mfma_f32_16x16x32_f16 v[138:141], v[102:105], v[142:145], v[138:141]
	s_waitcnt lgkmcnt(1)
	s_nop 0
	v_mfma_f32_16x16x32_f16 v[142:145], v[102:105], v[146:149], v[150:153]
	s_waitcnt lgkmcnt(0)
	s_nop 0
	v_mfma_f32_16x16x32_f16 v[146:149], v[102:105], v[154:157], v[158:161]
	s_nop 1
	v_cvt_pk_f16_f32 v1, v136, v137
	v_pk_max_f16 v1, v1, 0
	v_cvt_pk_f16_f32 v0, v134, v135
	v_pk_max_f16 v0, v0, 0
	v_cvt_pk_f16_f32 v135, v140, v141
	v_pk_max_f16 v135, v135, 0
	v_cvt_pk_f16_f32 v134, v138, v139
	v_pk_max_f16 v134, v134, 0
	ds_write2st64_b64 v218, v[0:1], v[134:135] offset1:8
	v_cvt_pk_f16_f32 v1, v144, v145
	v_pk_max_f16 v1, v1, 0
	v_cvt_pk_f16_f32 v0, v142, v143
	v_pk_max_f16 v0, v0, 0
	s_lshl_b32 s34, s2, 14
	v_cvt_pk_f16_f32 v135, v148, v149
	v_pk_max_f16 v135, v135, 0
	v_cvt_pk_f16_f32 v134, v146, v147
	v_pk_max_f16 v134, v134, 0
	s_or_b32 s34, s34, 0x18000
	ds_write2st64_b64 v218, v[0:1], v[134:135] offset0:16 offset1:24
	v_or_b32_e32 v172, s34, v197
	v_or_b32_e32 v223, s34, v198
	v_or_b32_e32 v143, s34, v199
	v_or_b32_e32 v142, s34, v200
	v_add_u32_e32 v0, s34, v208
	s_xor_b32 s34, s2, 1
	s_waitcnt vmcnt(2) lgkmcnt(0)
	s_barrier
	ds_read_b128 v[134:137], v201 offset:0
	s_mul_i32 s37, s34, 0xc000
	ds_read_b128 v[138:141], v202 offset:0
	ds_read_b128 v[144:147], v203 offset:0
	ds_read_b128 v[148:151], v204 offset:0
	v_add_u32_e32 v1, s37, v209
	ds_read_b128 v[152:155], v1 offset:0
	ds_read_b128 v[156:159], v1 offset:0x4000
	ds_read_b128 v[160:163], v1 offset:0x8000
	ds_read_b128 v[164:167], v1 offset:0x400
	ds_read_b128 v[168:171], v1 offset:0x4400
	ds_read_b128 v[174:177], v1 offset:0x8400
	ds_read_b128 v[178:181], v172 offset:0
	s_waitcnt lgkmcnt(10)
	v_subrev_u32_e32 v186, 56, v215
	v_mfma_f32_16x16x32_f16 v[182:185], v[2:5], v[134:137], v[118:121]
	v_min_u32_e32 v225, s17, v186
	v_mfma_f32_16x16x32_f16 v[186:189], v[42:45], v[134:137], v[122:125]
	ds_read_b128 v[226:229], v223 offset:0
	s_waitcnt lgkmcnt(10)
	v_mfma_f32_16x16x32_f16 v[134:137], v[66:69], v[134:137], v[126:129]
	v_lshl_or_b32 v173, v196, 8, v190
	v_mfma_f32_16x16x32_f16 v[182:185], v[6:9], v[138:141], v[182:185]
	v_add_u32_e32 v196, -8, v215
	v_min_u32_e32 v238, s17, v196
	v_subrev_u32_e32 v196, 52, v215
	v_mfma_f32_16x16x32_f16 v[186:189], v[46:49], v[138:141], v[186:189]
	v_add_u32_e32 v221, -4, v215
	v_min_u32_e32 v196, s18, v196
	v_min_u32_e32 v221, s18, v221
	v_mfma_f32_16x16x32_f16 v[230:233], v[70:73], v[138:141], v[134:137]
	s_cmp_lg_u32 s42, 0
	s_cbranch_scc1 .Lmp0_nofeat
	v_add_u32_e32 v224, s20, v216
	v_cmp_gt_u32_e32 vcc, s8, v224
	v_mov_b32_e32 v234, s16
	s_nop 0
	v_cndmask_b32_e32 v234, v234, v224, vcc
	v_lshlrev_b32_e32 v234, 5, v234
	global_load_dwordx4 v[134:137], v234, s[6:7]
	global_load_dwordx4 v[138:141], v234, s[6:7] offset:16

.LBB8_6:
	s_and_b64 s[24:25], s[6:7], exec
	s_cselect_b32 s23, 0xc000, 0
	s_add_i32 s24, s23, 0
	v_add3_u32 v27, s24, v36, v44
	ds_read_b128 v[52:55], v27
	ds_read_b128 v[56:59], v27 offset:16384
	ds_read_b128 v[60:63], v27 offset:32768
	ds_read_b128 v[64:67], v27 offset:1024
	ds_read_b128 v[68:71], v27 offset:17408
	s_andn2_b64 vcc, exec, s[0:1]
	s_waitcnt lgkmcnt(0)
	v_pk_add_f16 v56, v52, v56
	v_pk_add_f16 v57, v53, v57
	v_pk_add_f16 v58, v54, v58
	v_pk_add_f16 v59, v55, v59
	ds_read_b128 v[52:55], v27 offset:33792
	v_pk_add_f16 v59, v59, v63
	v_pk_add_f16 v58, v58, v62
	v_pk_add_f16 v57, v57, v61
	v_pk_add_f16 v56, v56, v60
	ds_write_b128 v27, v[56:59]
	v_pk_add_f16 v56, v64, v68
	v_pk_add_f16 v57, v65, v69
	v_pk_add_f16 v58, v66, v70
	v_pk_add_f16 v59, v67, v71
	s_waitcnt lgkmcnt(0)
	v_pk_add_f16 v54, v58, v54
	v_pk_add_f16 v55, v59, v55
	v_pk_add_f16 v53, v57, v53
	v_pk_add_f16 v52, v56, v52
	ds_write_b128 v27, v[52:55] offset:1024
	s_cbranch_vccnz .LBB8_5
	v_cvt_pk_f16_f32 v25, v24, v25
	v_cvt_pk_f16_f32 v24, v22, v23
	v_add_u32_e32 v27, s18, v30
	v_cmp_gt_i32_e32 vcc, s12, v27
	v_mov_b32_e32 v27, v26
	s_nop 0
	v_cndmask_b32_e32 v24, 0, v24, vcc
	v_cndmask_b32_e32 v25, 0, v25, vcc
	ds_write_b128 v28, v[24:27]
	s_branch .LBB8_5
